# K/V ring issue: LDS-DMA landing base (M0) formed on the scalar unit from a per-wave constant instead of v_add + v_readfirstlane per DMA
# baseline (speedup 1.0000x reference)
.LBB0_445:
	v_readfirstlane_b32 s96, v149
	v_readfirstlane_b32 s97, v158
	s_andn2_b64 vcc, exec, s[2:3]
	s_cbranch_vccnz .LBB0_447
	s_waitcnt vmcnt(8)

.LBB0_455:
	s_cmp_ge_u32 s22, s18
	s_cbranch_scc1 .Lring_issue_skip_2
	s_add_i32 s85, s2, 0x700
	s_mul_hi_i32 s86, s85, 0x3600
	s_mulk_i32 s85, 0x3600
	s_add_u32 s88, s14, s85
	s_addc_u32 s89, s15, s86
	s_add_u32 s90, s16, s85
	s_addc_u32 s91, s17, s86
	s_add_i32 s85, s30, 0x18000
	s_and_b32 s85, s85, 0x18000
	s_add_i32 s85, s85, 0
	s_add_i32 s86, s85, s96
	s_mov_b32 m0, s86
	s_add_i32 s87, s85, s97
	global_load_lds_dwordx4 v151, s[88:89]
	s_addk_i32 s87, 0x2000
	s_mov_b32 m0, s87
	s_add_i32 s87, s86, 0x4000
	global_load_lds_dwordx4 v153, s[88:89]
	s_mov_b32 m0, s87
	s_add_i32 s87, s86, 0x6000
	global_load_lds_dwordx4 v155, s[90:91]
	s_mov_b32 m0, s87
	s_nop 0
	global_load_lds_dwordx4 v157, s[90:91]

.LBB0_511:
	v_readfirstlane_b32 s97, v97
	s_add_i32 s2, s28, s21
	s_add_i32 s2, s2, -1
	s_cmp_lt_i32 s2, 2
	s_mov_b64 s[2:3], -1
	s_cbranch_scc0 .LBB0_517
	s_add_i32 s2, s26, s21
	s_cmp_lg_u32 s2, 2
	s_mov_b64 s[2:3], -1
	s_cbranch_scc0 .LBB0_514
	s_cmp_gt_u32 s32, 0
	s_cbranch_scc1 .Lw_win_0_hi
	s_waitcnt vmcnt(0)
	s_branch .Lw_win_0_done

.LBB0_527:
	s_cmp_gt_i32 s25, s17
	s_cbranch_scc1 .Lring_issue_skip_0
	s_add_i32 s85, s2, 0x700
	s_mul_hi_i32 s86, s85, 0x3600
	s_mulk_i32 s85, 0x3600
	s_add_u32 s88, s12, s85
	s_addc_u32 s89, s13, s86
	s_add_u32 s90, s14, s85
	s_addc_u32 s91, s15, s86
	s_add_i32 s85, s30, 0xc000
	s_and_b32 s85, s85, 0xc000
	s_add_i32 s85, s85, s97
	s_mov_b32 m0, s85
	s_addk_i32 s85, 0x2000
	global_load_lds_dwordx4 v95, s[88:89]
	s_mov_b32 m0, s85
	s_nop 0
	global_load_lds_dwordx4 v96, s[90:91]

.LBB0_670:
	v_readfirstlane_b32 s97, v127
	s_add_i32 s8, s4, s7
	s_cmp_lt_i32 s8, 2
	s_mov_b64 s[0:1], -1
	s_cbranch_scc0 .LBB0_676
	s_cmp_lg_u32 s8, 1
	s_cbranch_scc0 .LBB0_673
	s_waitcnt vmcnt(0)
	s_mov_b64 s[0:1], 0

.LBB0_678:
	s_barrier
	s_cmp_eq_u32 s3, 0
	s_cbranch_scc1 .LBB0_680
	s_flbit_i32_b32 s0, s3
	s_xor_b32 s0, s0, 31
	s_lshl_b32 s1, 1, s0
	s_andn2_b32 s3, s3, s1
	s_mul_i32 s8, s0, 0xd8000
	s_add_u32 s0, s17, s8
	s_addc_u32 s1, s18, 0
	s_add_u32 s8, s19, s8
	s_addc_u32 s9, s20, 0
	s_lshl_b32 s10, s4, 14
	s_and_b32 s10, s10, 0xc000
	s_xor_b32 s10, s10, 0x8000
	s_add_i32 s10, s10, s97
	s_mov_b32 m0, s10
	s_addk_i32 s10, 0x2000
	s_add_i32 s4, s4, 1
	global_load_lds_dwordx4 v132, s[0:1]
	s_mov_b32 m0, s10
	s_nop 0
	global_load_lds_dwordx4 v133, s[8:9]
	s_branch .LBB0_681

.LBB0_772:
	v_readfirstlane_b32 s97, v99
	s_add_i32 s0, s24, s18
	s_add_i32 s0, s0, -1
	s_cmp_lt_i32 s0, 2
	s_mov_b64 s[0:1], -1
	s_cbranch_scc0 .LBB0_778
	s_add_i32 s0, s22, s18
	s_cmp_lg_u32 s0, 2
	s_mov_b64 s[0:1], -1
	s_cbranch_scc0 .LBB0_775
	s_cmp_gt_u32 s32, 0
	s_cbranch_scc1 .Lw_swa_0_hi
	s_waitcnt vmcnt(0)
	s_branch .Lw_swa_0_done

.LBB0_788:
	s_cmp_gt_i32 s21, s13
	s_cbranch_scc1 .Lring_issue_skip_1
	s_add_i32 s85, s0, 0x700
	s_mul_hi_i32 s86, s85, 0x3600
	s_mulk_i32 s85, 0x3600
	s_add_u32 s88, s2, s85
	s_addc_u32 s89, s3, s86
	s_add_u32 s90, s10, s85
	s_addc_u32 s91, s11, s86
	s_add_i32 s85, s26, 0xc000
	s_and_b32 s85, s85, 0xc000
	s_add_i32 s85, s85, s97
	s_mov_b32 m0, s85
	s_addk_i32 s85, 0x2000
	global_load_lds_dwordx4 v97, s[88:89]
	s_mov_b32 m0, s85
	s_nop 0
	global_load_lds_dwordx4 v98, s[90:91]
